# weight-conversion filler routine: all 32 tile loads of a pass issued up front (was a 14-deep rolling window), counted waits recomputed; applies to the in-proj tail, top-k and FFN-phase conversion slot
# speedup vs baseline: 1.0076x; 1.0037x over previous
.Lfill_loop:
	v_lshl_or_b32 v194, s7, 18, v139
	v_lshl_add_u64 v[40:41], v[2:3], 0, v[194:195]
	v_add_co_u32_e32 v8, vcc, 0x1000, v40
	s_mov_b32 s8, 0xa000
	s_nop 1
	v_addc_co_u32_e32 v9, vcc, 0, v41, vcc
	v_add_co_u32_e32 v12, vcc, 0x2000, v40
	global_load_dwordx4 v[4:7], v[40:41], off nt
	s_nop 1
	v_addc_co_u32_e32 v13, vcc, 0, v41, vcc
	v_add_co_u32_e32 v16, vcc, 0x3000, v40
	global_load_dwordx4 v[8:11], v[8:9], off nt
	s_nop 1
	v_addc_co_u32_e32 v17, vcc, 0, v41, vcc
	v_add_co_u32_e32 v20, vcc, 0x4000, v40
	global_load_dwordx4 v[16:19], v[16:17], off nt
	s_nop 1
	v_addc_co_u32_e32 v21, vcc, 0, v41, vcc
	v_add_co_u32_e32 v24, vcc, 0x5000, v40
	global_load_dwordx4 v[20:23], v[20:21], off nt
	s_nop 1
	v_addc_co_u32_e32 v25, vcc, 0, v41, vcc
	v_add_co_u32_e32 v28, vcc, 0x6000, v40
	global_load_dwordx4 v[24:27], v[24:25], off nt
	s_nop 1
	v_addc_co_u32_e32 v29, vcc, 0, v41, vcc
	v_add_co_u32_e32 v32, vcc, 0x7000, v40
	global_load_dwordx4 v[12:15], v[12:13], off nt
	s_nop 1
	v_addc_co_u32_e32 v33, vcc, 0, v41, vcc
	v_add_co_u32_e32 v36, vcc, s9, v40
	global_load_dwordx4 v[32:35], v[32:33], off nt
	s_nop 1
	v_addc_co_u32_e32 v37, vcc, 0, v41, vcc
	v_add_co_u32_e32 v42, vcc, 0x9000, v40
	global_load_dwordx4 v[36:39], v[36:37], off nt
	s_nop 1
	v_addc_co_u32_e32 v43, vcc, 0, v41, vcc
	global_load_dwordx4 v[44:47], v[42:43], off nt
	v_add_co_u32_e32 v42, vcc, s8, v40
	s_mov_b32 s8, 0xe000
	s_nop 1
	v_addc_co_u32_e32 v43, vcc, 0, v41, vcc
	global_load_dwordx4 v[68:71], v[42:43], off nt
	v_add_co_u32_e32 v42, vcc, 0xb000, v40
	global_load_dwordx4 v[28:31], v[28:29], off nt
	s_nop 1
	v_addc_co_u32_e32 v43, vcc, 0, v41, vcc
	global_load_dwordx4 v[72:75], v[42:43], off nt
	v_add_co_u32_e32 v42, vcc, s16, v40
	s_nop 1
	v_addc_co_u32_e32 v43, vcc, 0, v41, vcc
	global_load_dwordx4 v[76:79], v[42:43], off nt
	v_add_co_u32_e32 v42, vcc, 0xd000, v40
	s_nop 1
	v_addc_co_u32_e32 v43, vcc, 0, v41, vcc
	global_load_dwordx4 v[80:83], v[42:43], off nt
	v_add_co_u32_e32 v42, vcc, s8, v40
	s_mov_b32 s8, 0x12000
	s_nop 1
	v_addc_co_u32_e32 v43, vcc, 0, v41, vcc
	global_load_dwordx4 v[84:87], v[42:43], off nt
	v_add_co_u32_e32 v42, vcc, 0xf000, v40
	s_nop 1
	v_addc_co_u32_e32 v43, vcc, 0, v41, vcc
	global_load_dwordx4 v[88:91], v[42:43], off nt
	v_add_co_u32_e32 v42, vcc, s73, v40
	s_nop 1
	v_addc_co_u32_e32 v43, vcc, 0, v41, vcc
	global_load_dwordx4 v[92:95], v[42:43], off nt
	v_add_co_u32_e32 v42, vcc, 0x11000, v40
	s_nop 1
	v_addc_co_u32_e32 v43, vcc, 0, v41, vcc
	global_load_dwordx4 v[96:99], v[42:43], off nt
	v_add_co_u32_e32 v42, vcc, s8, v40
	s_mov_b32 s8, 0x14000
	s_nop 1
	v_addc_co_u32_e32 v43, vcc, 0, v41, vcc
	global_load_dwordx4 v[140:143], v[42:43], off nt
	v_add_co_u32_e32 v42, vcc, 0x13000, v40
	s_nop 1
	v_addc_co_u32_e32 v43, vcc, 0, v41, vcc
	global_load_dwordx4 v[144:147], v[42:43], off nt
	v_add_co_u32_e32 v42, vcc, s8, v40
	s_mov_b32 s8, 0x1a000
	s_nop 1
	v_addc_co_u32_e32 v43, vcc, 0, v41, vcc
	global_load_dwordx4 v[148:151], v[42:43], off nt
	v_add_co_u32_e32 v42, vcc, 0x15000, v40
	s_nop 1
	v_addc_co_u32_e32 v43, vcc, 0, v41, vcc
	global_load_dwordx4 v[152:155], v[42:43], off nt
	v_add_co_u32_e32 v42, vcc, s13, v40
	s_nop 1
	v_addc_co_u32_e32 v43, vcc, 0, v41, vcc
	global_load_dwordx4 v[156:159], v[42:43], off nt
	v_add_co_u32_e32 v42, vcc, 0x17000, v40
	s_nop 1
	v_addc_co_u32_e32 v43, vcc, 0, v41, vcc
	global_load_dwordx4 v[160:163], v[42:43], off nt
	v_add_co_u32_e32 v42, vcc, s14, v40
	s_nop 1
	v_addc_co_u32_e32 v43, vcc, 0, v41, vcc
	global_load_dwordx4 v[164:167], v[42:43], off nt
	v_add_co_u32_e32 v42, vcc, 0x19000, v40
	s_nop 1
	v_addc_co_u32_e32 v43, vcc, 0, v41, vcc
	global_load_dwordx4 v[168:171], v[42:43], off nt
	v_add_co_u32_e32 v42, vcc, s8, v40
	s_mov_b32 s8, 0x1c000
	s_nop 1
	v_addc_co_u32_e32 v43, vcc, 0, v41, vcc
	global_load_dwordx4 v[172:175], v[42:43], off nt
	v_add_co_u32_e32 v42, vcc, 0x1b000, v40
	s_nop 1
	v_addc_co_u32_e32 v43, vcc, 0, v41, vcc
	global_load_dwordx4 v[176:179], v[42:43], off nt
	v_add_co_u32_e32 v42, vcc, s8, v40
	s_nop 1
	v_addc_co_u32_e32 v43, vcc, 0, v41, vcc
	global_load_dwordx4 v[180:183], v[42:43], off nt
	v_add_co_u32_e32 v42, vcc, 0x1d000, v40
	s_nop 1
	v_addc_co_u32_e32 v43, vcc, 0, v41, vcc
	global_load_dwordx4 v[184:187], v[42:43], off nt
	v_add_co_u32_e32 v42, vcc, s15, v40
	s_nop 1
	v_addc_co_u32_e32 v43, vcc, 0, v41, vcc
	v_add_co_u32_e32 v40, vcc, 0x1f000, v40
	global_load_dwordx4 v[188:191], v[42:43], off nt
	s_nop 1
	v_addc_co_u32_e32 v41, vcc, 0, v41, vcc
	global_load_dwordx4 v[196:199], v[40:41], off nt
	s_nop 1
	s_nop 0
	s_nop 0
	s_nop 0
	s_nop 0
	s_nop 0
	s_nop 0
	s_nop 0
	s_nop 0
	s_nop 0
	s_nop 0
	s_nop 0
	s_nop 1
	s_lshl_b32 s7, s7, 2
	s_nop 0
	s_waitcnt vmcnt(31)
	v_pk_mul_f32 v[122:123], v[4:5], s[18:19] op_sel_hi:[1,0]
	s_nop 0
	s_waitcnt vmcnt(30)
	v_pk_mul_f32 v[126:127], v[8:9], s[18:19] op_sel_hi:[1,0]
	s_waitcnt vmcnt(28)
	v_pk_mul_f32 v[114:115], v[20:21], s[18:19] op_sel_hi:[1,0]
	s_waitcnt vmcnt(27)
	v_pk_mul_f32 v[54:55], v[26:27], s[18:19] op_sel_hi:[1,0]
	s_nop 0
	s_nop 1
	v_pk_mul_f32 v[118:119], v[24:25], s[18:19] op_sel_hi:[1,0]
	s_nop 0
	s_nop 0
	s_waitcnt vmcnt(25)
	v_pk_mul_f32 v[124:125], v[32:33], s[18:19] op_sel_hi:[1,0]
	s_waitcnt vmcnt(24)
	v_pk_mul_f32 v[106:107], v[36:37], s[18:19] op_sel_hi:[1,0]
	s_waitcnt vmcnt(23)
	v_pk_mul_f32 v[110:111], v[44:45], s[18:19] op_sel_hi:[1,0]
	s_waitcnt vmcnt(19)
	v_pk_mul_f32 v[100:101], v[76:77], s[18:19] op_sel_hi:[1,0]
	s_nop 1
	v_pk_mul_f32 v[128:129], v[12:13], s[18:19] op_sel_hi:[1,0]
	s_nop 0
	s_nop 0
	s_waitcnt vmcnt(18)
	v_pk_mul_f32 v[102:103], v[80:81], s[18:19] op_sel_hi:[1,0]
	s_nop 1
	v_pk_mul_f32 v[130:131], v[16:17], s[18:19] op_sel_hi:[1,0]
	s_nop 0
	s_nop 1
	v_pk_mul_f32 v[120:121], v[28:29], s[18:19] op_sel_hi:[1,0]
	s_nop 0
	s_waitcnt vmcnt(15)
	v_pk_mul_f32 v[26:27], v[94:95], s[18:19] op_sel_hi:[1,0]
	s_nop 0
	s_waitcnt vmcnt(14)
	v_pk_mul_f32 v[94:95], v[96:97], s[18:19] op_sel_hi:[1,0]
	v_pk_mul_f32 v[112:113], v[68:69], s[18:19] op_sel_hi:[1,0]
	s_waitcnt vmcnt(13)
	v_pk_mul_f32 v[32:33], v[142:143], s[18:19] op_sel_hi:[1,0]
	v_pk_mul_f32 v[96:97], v[140:141], s[18:19] op_sel_hi:[1,0]
	v_mov_b32_e32 v140, v195
	v_mov_b32_e32 v141, v195
	v_mov_b32_e32 v142, v195
	v_mov_b32_e32 v143, v195
	v_cvt_pk_fp8_f32 v140, v122, v126
	v_cvt_pk_fp8_f32 v141, v114, v118
	v_cvt_pk_fp8_f32 v142, v106, v110
	v_cvt_pk_fp8_f32 v143, v100, v102
	v_pk_mul_f32 v[116:117], v[72:73], s[18:19] op_sel_hi:[1,0]
	v_pk_mul_f32 v[104:105], v[84:85], s[18:19] op_sel_hi:[1,0]
	v_pk_mul_f32 v[108:109], v[88:89], s[18:19] op_sel_hi:[1,0]
	v_cvt_pk_fp8_f32 v140, v128, v130 op_sel:[0,0,1]
	v_cvt_pk_fp8_f32 v141, v120, v124 op_sel:[0,0,1]
	v_cvt_pk_fp8_f32 v142, v112, v116 op_sel:[0,0,1]
	v_cvt_pk_fp8_f32 v143, v104, v108 op_sel:[0,0,1]
	v_bitop3_b32 v100, s7, v133, v134 bitop3:0x36
	v_lshl_add_u32 v100, v100, 4, v138
	v_pk_mul_f32 v[44:45], v[90:91], s[18:19] op_sel_hi:[1,0]
	v_pk_mul_f32 v[90:91], v[92:93], s[18:19] op_sel_hi:[1,0]
	ds_write_b128 v100, v[140:143]
	v_mov_b32_e32 v140, v195
	v_cvt_pk_fp8_f32 v140, v90, v94
	v_mov_b32_e32 v90, v195
	v_pk_mul_f32 v[42:43], v[38:39], s[18:19] op_sel_hi:[1,0]
	v_pk_mul_f32 v[38:39], v[82:83], s[18:19] op_sel_hi:[1,0]
	v_pk_mul_f32 v[40:41], v[86:87], s[18:19] op_sel_hi:[1,0]
	s_waitcnt vmcnt(11)
	v_pk_mul_f32 v[82:83], v[148:149], s[18:19] op_sel_hi:[1,0]
	s_waitcnt vmcnt(10)
	v_pk_mul_f32 v[86:87], v[152:153], s[18:19] op_sel_hi:[1,0]
	v_cvt_pk_fp8_f32 v90, v91, v95
	v_mov_b32_e32 v91, v195
	v_pk_mul_f32 v[48:49], v[70:71], s[18:19] op_sel_hi:[1,0]
	v_mov_b32_e32 v143, v195
	v_cvt_pk_fp8_f32 v91, v83, v87
	v_pk_mul_f32 v[56:57], v[30:31], s[18:19] op_sel_hi:[1,0]
	v_pk_mul_f32 v[30:31], v[98:99], s[18:19] op_sel_hi:[1,0]
	v_pk_mul_f32 v[98:99], v[144:145], s[18:19] op_sel_hi:[1,0]
	s_waitcnt vmcnt(9)
	v_pk_mul_f32 v[88:89], v[156:157], s[18:19] op_sel_hi:[1,0]
	s_waitcnt vmcnt(8)
	v_pk_mul_f32 v[92:93], v[160:161], s[18:19] op_sel_hi:[1,0]
	v_or_b32_e32 v144, s7, v134
	v_cvt_pk_fp8_f32 v91, v89, v93 op_sel:[0,0,1]
	v_mov_b32_e32 v93, v195
	v_pk_mul_f32 v[58:59], v[6:7], s[18:19] op_sel_hi:[1,0]
	v_pk_mul_f32 v[62:63], v[10:11], s[18:19] op_sel_hi:[1,0]
	v_pk_mul_f32 v[50:51], v[22:23], s[18:19] op_sel_hi:[1,0]
	v_pk_mul_f32 v[46:47], v[46:47], s[18:19] op_sel_hi:[1,0]
	v_pk_mul_f32 v[36:37], v[78:79], s[18:19] op_sel_hi:[1,0]
	v_pk_mul_f32 v[64:65], v[14:15], s[18:19] op_sel_hi:[1,0]
	v_pk_mul_f32 v[66:67], v[18:19], s[18:19] op_sel_hi:[1,0]
	v_pk_mul_f32 v[60:61], v[34:35], s[18:19] op_sel_hi:[1,0]
	v_pk_mul_f32 v[52:53], v[74:75], s[18:19] op_sel_hi:[1,0]
	v_mov_b32_e32 v122, v195
	v_pk_mul_f32 v[18:19], v[150:151], s[18:19] op_sel_hi:[1,0]
	v_pk_mul_f32 v[22:23], v[154:155], s[18:19] op_sel_hi:[1,0]
	v_mov_b32_e32 v141, v195
	v_cvt_pk_fp8_f32 v122, v123, v127
	v_mov_b32_e32 v123, v195
	v_cvt_pk_fp8_f32 v141, v82, v86
	v_cvt_pk_fp8_f32 v123, v115, v119
	s_waitcnt vmcnt(3)
	v_pk_mul_f32 v[68:69], v[180:181], s[18:19] op_sel_hi:[1,0]
	v_pk_mul_f32 v[24:25], v[158:159], s[18:19] op_sel_hi:[1,0]
	v_pk_mul_f32 v[28:29], v[162:163], s[18:19] op_sel_hi:[1,0]
	v_pk_mul_f32 v[10:11], v[166:167], s[18:19] op_sel_hi:[1,0]
	v_pk_mul_f32 v[74:75], v[164:165], s[18:19] op_sel_hi:[1,0]
	v_pk_mul_f32 v[14:15], v[170:171], s[18:19] op_sel_hi:[1,0]
	s_waitcnt vmcnt(2)
	v_pk_mul_f32 v[70:71], v[184:185], s[18:19] op_sel_hi:[1,0]
	v_pk_mul_f32 v[78:79], v[168:169], s[18:19] op_sel_hi:[1,0]
	v_cvt_pk_fp8_f32 v143, v68, v70
	v_bitop3_b32 v68, v144, v133, 1 bitop3:0x36
	v_cvt_pk_fp8_f32 v93, v69, v71
	v_mov_b32_e32 v69, v195
	v_mov_b32_e32 v70, v195
	v_mov_b32_e32 v71, v195
	s_waitcnt vmcnt(1)
	v_pk_mul_f32 v[72:73], v[188:189], s[18:19] op_sel_hi:[1,0]
	v_cvt_pk_fp8_f32 v69, v50, v54
	v_cvt_pk_fp8_f32 v70, v42, v46
	s_waitcnt vmcnt(0)
	v_pk_mul_f32 v[76:77], v[196:197], s[18:19] op_sel_hi:[1,0]
	v_cvt_pk_fp8_f32 v71, v36, v38
	v_cvt_pk_fp8_f32 v143, v72, v76 op_sel:[0,0,1]
	v_lshl_add_u32 v72, v68, 4, v138
	v_mov_b32_e32 v68, v195
	v_cvt_pk_fp8_f32 v68, v58, v62
	v_cvt_pk_fp8_f32 v69, v56, v60 op_sel:[0,0,1]
	v_cvt_pk_fp8_f32 v70, v48, v52 op_sel:[0,0,1]
	v_cvt_pk_fp8_f32 v71, v40, v44 op_sel:[0,0,1]
	v_cvt_pk_fp8_f32 v68, v64, v66 op_sel:[0,0,1]
	v_mov_b32_e32 v58, v195
	v_cvt_pk_fp8_f32 v58, v59, v63
	v_mov_b32_e32 v59, v195
	ds_write_b128 v100, v[68:71] offset:256
	v_mov_b32_e32 v68, v195
	v_cvt_pk_fp8_f32 v68, v26, v30
	v_mov_b32_e32 v26, v195
	v_mov_b32_e32 v69, v195
	v_cvt_pk_fp8_f32 v26, v27, v31
	v_mov_b32_e32 v27, v195
	v_cvt_pk_fp8_f32 v69, v18, v22
	v_cvt_pk_fp8_f32 v59, v51, v55
	v_cvt_pk_fp8_f32 v27, v19, v23
	v_pk_mul_f32 v[4:5], v[182:183], s[18:19] op_sel_hi:[1,0]
	v_pk_mul_f32 v[6:7], v[186:187], s[18:19] op_sel_hi:[1,0]
	v_cvt_pk_fp8_f32 v141, v88, v92 op_sel:[0,0,1]
	v_mov_b32_e32 v142, v195
	v_cvt_pk_fp8_f32 v123, v121, v125 op_sel:[0,0,1]
	v_mov_b32_e32 v124, v195
	v_mov_b32_e32 v125, v195
	v_mov_b32_e32 v92, v195
	v_cvt_pk_fp8_f32 v69, v24, v28 op_sel:[0,0,1]
	v_mov_b32_e32 v70, v195
	v_mov_b32_e32 v71, v195
	v_cvt_pk_fp8_f32 v59, v57, v61 op_sel:[0,0,1]
	v_mov_b32_e32 v60, v195
	v_mov_b32_e32 v61, v195
	v_cvt_pk_fp8_f32 v27, v25, v29 op_sel:[0,0,1]
	v_mov_b32_e32 v28, v195
	v_mov_b32_e32 v29, v195
	v_cvt_pk_fp8_f32 v142, v74, v78
	v_cvt_pk_fp8_f32 v124, v107, v111
	v_cvt_pk_fp8_f32 v125, v101, v103
	v_cvt_pk_fp8_f32 v92, v75, v79
	v_cvt_pk_fp8_f32 v70, v10, v14
	v_cvt_pk_fp8_f32 v71, v4, v6
	v_cvt_pk_fp8_f32 v60, v43, v47
	v_cvt_pk_fp8_f32 v61, v37, v39
	v_cvt_pk_fp8_f32 v28, v11, v15
	v_cvt_pk_fp8_f32 v29, v5, v7
	v_pk_mul_f32 v[34:35], v[146:147], s[18:19] op_sel_hi:[1,0]
	v_pk_mul_f32 v[16:17], v[174:175], s[18:19] op_sel_hi:[1,0]
	v_pk_mul_f32 v[80:81], v[172:173], s[18:19] op_sel_hi:[1,0]
	v_pk_mul_f32 v[20:21], v[178:179], s[18:19] op_sel_hi:[1,0]
	v_pk_mul_f32 v[84:85], v[176:177], s[18:19] op_sel_hi:[1,0]
	v_pk_mul_f32 v[8:9], v[190:191], s[18:19] op_sel_hi:[1,0]
	v_pk_mul_f32 v[12:13], v[198:199], s[18:19] op_sel_hi:[1,0]
	v_cvt_pk_fp8_f32 v140, v96, v98 op_sel:[0,0,1]
	v_cvt_pk_fp8_f32 v142, v80, v84 op_sel:[0,0,1]
	v_cvt_pk_fp8_f32 v122, v129, v131 op_sel:[0,0,1]
	v_cvt_pk_fp8_f32 v124, v113, v117 op_sel:[0,0,1]
	v_cvt_pk_fp8_f32 v125, v105, v109 op_sel:[0,0,1]
	v_cvt_pk_fp8_f32 v90, v97, v99 op_sel:[0,0,1]
	v_cvt_pk_fp8_f32 v92, v81, v85 op_sel:[0,0,1]
	v_cvt_pk_fp8_f32 v93, v73, v77 op_sel:[0,0,1]
	v_cvt_pk_fp8_f32 v68, v32, v34 op_sel:[0,0,1]
	v_cvt_pk_fp8_f32 v70, v16, v20 op_sel:[0,0,1]
	v_cvt_pk_fp8_f32 v71, v8, v12 op_sel:[0,0,1]
	v_cvt_pk_fp8_f32 v58, v65, v67 op_sel:[0,0,1]
	v_cvt_pk_fp8_f32 v60, v49, v53 op_sel:[0,0,1]
	v_cvt_pk_fp8_f32 v61, v41, v45 op_sel:[0,0,1]
	v_cvt_pk_fp8_f32 v26, v33, v35 op_sel:[0,0,1]
	v_cvt_pk_fp8_f32 v28, v17, v21 op_sel:[0,0,1]
	v_cvt_pk_fp8_f32 v29, v9, v13 op_sel:[0,0,1]
	s_mov_b32 s7, 1
	s_and_b64 vcc, exec, s[0:1]
	s_mov_b64 s[0:1], 0
	ds_write_b128 v72, v[140:143]
	ds_write_b128 v100, v[122:125] offset:128
	ds_write_b128 v72, v[90:93] offset:128
	ds_write_b128 v72, v[68:71] offset:256
	ds_write_b128 v100, v[58:61] offset:384
	ds_write_b128 v72, v[26:29] offset:384
	s_cbranch_vccnz .Lfill_loop
	s_lshl_b32 s0, s3, 10
	s_waitcnt lgkmcnt(0)
	v_mov_b32_e32 v10, v132
	s_or_b32 s0, s0, s5
	s_mulk_i32 s0, 0xb00
	v_ashrrev_i32_e32 v11, 3, v10
	v_lshrrev_b32_e32 v5, 2, v11
	s_add_u32 s0, s10, s0
	v_xor_b32_e32 v5, v5, v10
	s_addc_u32 s1, s11, 0
	v_lshlrev_b32_e32 v5, 4, v5
	s_add_u32 s0, s0, s2
	v_lshlrev_b32_e32 v4, 7, v11
	v_and_b32_e32 v12, 0x70, v5
	v_readlane_b32 s2, v253, 56
	v_lshlrev_b32_e32 v2, 4, v10
	s_addc_u32 s1, s1, s4
	v_add3_u32 v4, s2, v4, v12
	ds_read_b128 v[4:7], v4
	v_and_b32_e32 v194, 0x70, v2
	v_lshl_add_u64 v[2:3], s[0:1], 0, v[194:195]
	s_mov_b64 s[0:1], 0xbc00000
	v_lshl_add_u64 v[2:3], v[2:3], 0, s[0:1]
	s_movk_i32 s3, 0xb00
	v_mad_i64_i32 v[8:9], s[0:1], v11, s3, v[2:3]
	s_waitcnt lgkmcnt(0)
	global_store_dwordx4 v[8:9], v[4:7], off nt
	v_add_u32_e32 v8, 8, v11
	s_nop 0
	v_lshrrev_b32_e32 v5, 2, v8
	v_xor_b32_e32 v5, v5, v10
	v_lshlrev_b32_e32 v5, 4, v5
	v_lshlrev_b32_e32 v4, 7, v8
	v_and_b32_e32 v5, 0x70, v5
	v_add3_u32 v4, s2, v4, v5
	ds_read_b128 v[4:7], v4
	v_mad_i64_i32 v[8:9], s[0:1], v8, s3, v[2:3]
	s_waitcnt lgkmcnt(0)
	global_store_dwordx4 v[8:9], v[4:7], off nt
	v_add_u32_e32 v8, 16, v11
	s_nop 0
	v_lshrrev_b32_e32 v5, 2, v8
	v_xor_b32_e32 v5, v5, v10
	v_lshlrev_b32_e32 v5, 4, v5
	v_lshlrev_b32_e32 v4, 7, v8
	v_and_b32_e32 v5, 0x70, v5
	v_add3_u32 v4, s2, v4, v5
	ds_read_b128 v[4:7], v4
	v_mad_i64_i32 v[8:9], s[0:1], v8, s3, v[2:3]
	s_waitcnt lgkmcnt(0)
	global_store_dwordx4 v[8:9], v[4:7], off nt
	v_add_u32_e32 v8, 24, v11
	s_nop 0
	v_lshrrev_b32_e32 v5, 2, v8
	v_xor_b32_e32 v5, v5, v10
	v_lshlrev_b32_e32 v5, 4, v5
	v_lshlrev_b32_e32 v4, 7, v8
	v_and_b32_e32 v5, 0x70, v5
	v_add3_u32 v4, s2, v4, v5
	ds_read_b128 v[4:7], v4
	v_mad_i64_i32 v[8:9], s[0:1], v8, s3, v[2:3]
	s_waitcnt lgkmcnt(0)
	global_store_dwordx4 v[8:9], v[4:7], off nt
	v_add_u32_e32 v8, 32, v11
	s_nop 0
	v_lshlrev_b32_e32 v4, 7, v8
	v_add3_u32 v4, s2, v4, v12
	ds_read_b128 v[4:7], v4
	v_mad_i64_i32 v[8:9], s[0:1], v8, s3, v[2:3]
	s_waitcnt lgkmcnt(0)
	global_store_dwordx4 v[8:9], v[4:7], off nt
	v_add_u32_e32 v8, 40, v11
	s_nop 0
	v_lshrrev_b32_e32 v5, 2, v8
	v_xor_b32_e32 v5, v5, v10
	v_lshlrev_b32_e32 v5, 4, v5
	v_lshlrev_b32_e32 v4, 7, v8
	v_and_b32_e32 v5, 0x70, v5
	v_add3_u32 v4, s2, v4, v5
	ds_read_b128 v[4:7], v4
	v_mad_i64_i32 v[8:9], s[0:1], v8, s3, v[2:3]
	s_waitcnt lgkmcnt(0)
	global_store_dwordx4 v[8:9], v[4:7], off nt
	v_add_u32_e32 v8, 48, v11
	s_nop 0
	v_lshrrev_b32_e32 v5, 2, v8
	v_xor_b32_e32 v5, v5, v10
	v_lshlrev_b32_e32 v5, 4, v5
	v_lshlrev_b32_e32 v4, 7, v8
	v_and_b32_e32 v5, 0x70, v5
	v_add3_u32 v4, s2, v4, v5
	ds_read_b128 v[4:7], v4
	v_mad_i64_i32 v[8:9], s[0:1], v8, s3, v[2:3]
	s_waitcnt lgkmcnt(0)
	global_store_dwordx4 v[8:9], v[4:7], off nt
	v_add_u32_e32 v8, 56, v11
	s_nop 0
	v_lshrrev_b32_e32 v5, 2, v8
	v_xor_b32_e32 v5, v5, v10
	v_lshlrev_b32_e32 v5, 4, v5
	v_lshlrev_b32_e32 v4, 7, v8
	v_and_b32_e32 v5, 0x70, v5
	v_add3_u32 v4, s2, v4, v5
	ds_read_b128 v[4:7], v4
	v_mad_i64_i32 v[8:9], s[0:1], v8, s3, v[2:3]
	s_waitcnt lgkmcnt(0)
	global_store_dwordx4 v[8:9], v[4:7], off nt
	v_add_u32_e32 v8, 64, v11
	s_nop 0
	v_lshlrev_b32_e32 v4, 7, v8
	v_add3_u32 v4, s2, v4, v12
	ds_read_b128 v[4:7], v4
	v_mad_i64_i32 v[8:9], s[0:1], v8, s3, v[2:3]
	s_waitcnt lgkmcnt(0)
	global_store_dwordx4 v[8:9], v[4:7], off nt
	v_add_u32_e32 v8, 0x48, v11
	s_nop 0
	v_lshrrev_b32_e32 v5, 2, v8
	v_xor_b32_e32 v5, v5, v10
	v_lshlrev_b32_e32 v5, 4, v5
	v_lshlrev_b32_e32 v4, 7, v8
	v_and_b32_e32 v5, 0x70, v5
	v_add3_u32 v4, s2, v4, v5
	ds_read_b128 v[4:7], v4
	v_mad_i64_i32 v[8:9], s[0:1], v8, s3, v[2:3]
	s_waitcnt lgkmcnt(0)
	global_store_dwordx4 v[8:9], v[4:7], off nt
	v_add_u32_e32 v8, 0x50, v11
	s_nop 0
	v_lshrrev_b32_e32 v5, 2, v8
	v_xor_b32_e32 v5, v5, v10
	v_lshlrev_b32_e32 v5, 4, v5
	v_lshlrev_b32_e32 v4, 7, v8
	v_and_b32_e32 v5, 0x70, v5
	v_add3_u32 v4, s2, v4, v5
	ds_read_b128 v[4:7], v4
	v_mad_i64_i32 v[8:9], s[0:1], v8, s3, v[2:3]
	s_waitcnt lgkmcnt(0)
	global_store_dwordx4 v[8:9], v[4:7], off nt
	v_add_u32_e32 v8, 0x58, v11
	s_nop 0
	v_lshrrev_b32_e32 v5, 2, v8
	v_xor_b32_e32 v5, v5, v10
	v_lshlrev_b32_e32 v5, 4, v5
	v_lshlrev_b32_e32 v4, 7, v8
	v_and_b32_e32 v5, 0x70, v5
	v_add3_u32 v4, s2, v4, v5
	ds_read_b128 v[4:7], v4
	v_mad_i64_i32 v[8:9], s[0:1], v8, s3, v[2:3]
	s_waitcnt lgkmcnt(0)
	global_store_dwordx4 v[8:9], v[4:7], off nt
	v_add_u32_e32 v8, 0x60, v11
	s_nop 0
	v_lshlrev_b32_e32 v4, 7, v8
	v_add3_u32 v4, s2, v4, v12
	ds_read_b128 v[4:7], v4
	v_mad_i64_i32 v[8:9], s[0:1], v8, s3, v[2:3]
	s_waitcnt lgkmcnt(0)
	global_store_dwordx4 v[8:9], v[4:7], off nt
	v_add_u32_e32 v8, 0x68, v11
	s_nop 0
	v_lshrrev_b32_e32 v5, 2, v8
	v_xor_b32_e32 v5, v5, v10
	v_lshlrev_b32_e32 v5, 4, v5
	v_lshlrev_b32_e32 v4, 7, v8
	v_and_b32_e32 v5, 0x70, v5
	v_add3_u32 v4, s2, v4, v5
	ds_read_b128 v[4:7], v4
	v_mad_i64_i32 v[8:9], s[0:1], v8, s3, v[2:3]
	s_waitcnt lgkmcnt(0)
	global_store_dwordx4 v[8:9], v[4:7], off nt
	v_add_u32_e32 v8, 0x70, v11
	s_nop 0
	v_lshrrev_b32_e32 v5, 2, v8
	v_xor_b32_e32 v5, v5, v10
	v_lshlrev_b32_e32 v5, 4, v5
	v_lshlrev_b32_e32 v4, 7, v8
	v_and_b32_e32 v5, 0x70, v5
	v_add3_u32 v4, s2, v4, v5
	ds_read_b128 v[4:7], v4
	v_mad_i64_i32 v[8:9], s[0:1], v8, s3, v[2:3]
	s_waitcnt lgkmcnt(0)
	global_store_dwordx4 v[8:9], v[4:7], off nt
	v_add_u32_e32 v8, 0x78, v11
	s_nop 0
	v_lshrrev_b32_e32 v5, 2, v8
	v_xor_b32_e32 v5, v5, v10
	v_lshlrev_b32_e32 v5, 4, v5
	v_lshlrev_b32_e32 v4, 7, v8
	v_and_b32_e32 v5, 0x70, v5
	v_add3_u32 v4, s2, v4, v5
	ds_read_b128 v[4:7], v4
	v_mad_i64_i32 v[2:3], s[0:1], v8, s3, v[2:3]
	s_mov_b64 s[0:1], 0
	s_waitcnt lgkmcnt(0)
	global_store_dwordx4 v[2:3], v[4:7], off nt
	s_waitcnt lgkmcnt(0)

.LBB0_889:
	v_or_b32_e32 v2, s17, v135
	v_mul_u32_u24_e32 v194, 0x2c00, v2
	v_lshl_add_u64 v[2:3], v[130:131], 0, v[194:195]
	global_load_dwordx4 v[126:129], v[2:3], off nt
	v_add_co_u32_e32 v4, vcc, 0x2000, v2
	s_xor_b64 s[6:7], s[8:9], -1
	s_nop 1
	v_addc_co_u32_e32 v5, vcc, 0, v3, vcc
	global_load_dwordx4 v[122:125], v[4:5], off offset:3072 nt
	v_add_co_u32_e32 v4, vcc, 0x5000, v2
	s_mov_b32 s8, 0x8000
	s_nop 1
	v_addc_co_u32_e32 v5, vcc, 0, v3, vcc
	global_load_dwordx4 v[118:121], v[4:5], off offset:2048 nt
	v_add_co_u32_e32 v4, vcc, s8, v2
	s_mov_b32 s8, 0x18000
	s_nop 1
	v_addc_co_u32_e32 v5, vcc, 0, v3, vcc
	global_load_dwordx4 v[114:117], v[4:5], off offset:1024 nt
	v_add_co_u32_e32 v4, vcc, 0xb000, v2
	s_nop 1
	v_addc_co_u32_e32 v5, vcc, 0, v3, vcc
	global_load_dwordx4 v[110:113], v[4:5], off nt
	v_add_co_u32_e32 v4, vcc, 0xd000, v2
	s_nop 1
	v_addc_co_u32_e32 v5, vcc, 0, v3, vcc
	global_load_dwordx4 v[106:109], v[4:5], off offset:3072 nt
	v_add_co_u32_e32 v4, vcc, s73, v2
	s_nop 1
	v_addc_co_u32_e32 v5, vcc, 0, v3, vcc
	global_load_dwordx4 v[102:105], v[4:5], off offset:2048 nt
	v_add_co_u32_e32 v4, vcc, 0x13000, v2
	s_nop 1
	v_addc_co_u32_e32 v5, vcc, 0, v3, vcc
	global_load_dwordx4 v[98:101], v[4:5], off offset:1024 nt
	v_add_co_u32_e32 v4, vcc, s18, v2
	s_nop 1
	v_addc_co_u32_e32 v5, vcc, 0, v3, vcc
	global_load_dwordx4 v[94:97], v[4:5], off nt
	v_add_co_u32_e32 v4, vcc, s8, v2
	s_nop 1
	v_addc_co_u32_e32 v5, vcc, 0, v3, vcc
	global_load_dwordx4 v[90:93], v[4:5], off offset:3072 nt
	v_add_co_u32_e32 v4, vcc, 0x1b000, v2
	s_nop 1
	v_addc_co_u32_e32 v5, vcc, 0, v3, vcc
	global_load_dwordx4 v[86:89], v[4:5], off offset:2048 nt
	v_add_co_u32_e32 v4, vcc, s19, v2
	s_nop 1
	v_addc_co_u32_e32 v5, vcc, 0, v3, vcc
	global_load_dwordx4 v[82:85], v[4:5], off offset:1024 nt
	v_add_co_u32_e32 v4, vcc, 0x21000, v2
	s_nop 1
	v_addc_co_u32_e32 v5, vcc, 0, v3, vcc
	global_load_dwordx4 v[78:81], v[4:5], off nt
	v_add_co_u32_e32 v4, vcc, 0x23000, v2
	s_nop 1
	v_addc_co_u32_e32 v5, vcc, 0, v3, vcc
	global_load_dwordx4 v[74:77], v[4:5], off offset:3072 nt
	v_add_co_u32_e32 v4, vcc, 0x26000, v2
	s_nop 1
	v_addc_co_u32_e32 v5, vcc, 0, v3, vcc
	global_load_dwordx4 v[70:73], v[4:5], off offset:2048 nt
	v_add_co_u32_e32 v4, vcc, 0x29000, v2
	s_nop 1
	v_addc_co_u32_e32 v5, vcc, 0, v3, vcc
	global_load_dwordx4 v[66:69], v[4:5], off offset:1024 nt
	s_nop 1
	s_mov_b32 s8, 0x2c000
	v_add_co_u32_e32 v4, vcc, s8, v2
	s_nop 1
	v_addc_co_u32_e32 v5, vcc, 0, v3, vcc
	global_load_dwordx4 v[62:65], v[4:5], off nt
	s_nop 1
	v_add_co_u32_e32 v4, vcc, 0x2e000, v2
	s_nop 1
	v_addc_co_u32_e32 v5, vcc, 0, v3, vcc
	global_load_dwordx4 v[58:61], v[4:5], off offset:3072 nt
	s_nop 1
	v_add_co_u32_e32 v4, vcc, 0x31000, v2
	s_nop 1
	v_addc_co_u32_e32 v5, vcc, 0, v3, vcc
	global_load_dwordx4 v[54:57], v[4:5], off offset:2048 nt
	s_nop 1
	v_add_co_u32_e32 v4, vcc, 0x34000, v2
	s_nop 1
	v_addc_co_u32_e32 v5, vcc, 0, v3, vcc
	global_load_dwordx4 v[50:53], v[4:5], off offset:1024 nt
	s_nop 1
	v_add_co_u32_e32 v4, vcc, 0x37000, v2
	s_nop 1
	v_addc_co_u32_e32 v5, vcc, 0, v3, vcc
	global_load_dwordx4 v[46:49], v[4:5], off nt
	s_nop 1
	v_add_co_u32_e32 v4, vcc, 0x39000, v2
	s_nop 1
	v_addc_co_u32_e32 v5, vcc, 0, v3, vcc
	global_load_dwordx4 v[42:45], v[4:5], off offset:3072 nt
	s_nop 1
	v_add_co_u32_e32 v4, vcc, 0x3c000, v2
	s_nop 1
	v_addc_co_u32_e32 v5, vcc, 0, v3, vcc
	global_load_dwordx4 v[38:41], v[4:5], off offset:2048 nt
	s_nop 1
	v_add_co_u32_e32 v4, vcc, 0x3f000, v2
	s_nop 1
	v_addc_co_u32_e32 v5, vcc, 0, v3, vcc
	global_load_dwordx4 v[34:37], v[4:5], off offset:1024 nt
	s_nop 1
	v_add_co_u32_e32 v4, vcc, 0x42000, v2
	s_nop 1
	v_addc_co_u32_e32 v5, vcc, 0, v3, vcc
	global_load_dwordx4 v[30:33], v[4:5], off nt
	s_nop 1
	v_add_co_u32_e32 v4, vcc, 0x44000, v2
	s_nop 1
	v_addc_co_u32_e32 v5, vcc, 0, v3, vcc
	global_load_dwordx4 v[26:29], v[4:5], off offset:3072 nt
	s_nop 1
	v_add_co_u32_e32 v4, vcc, 0x47000, v2
	s_nop 1
	v_addc_co_u32_e32 v5, vcc, 0, v3, vcc
	global_load_dwordx4 v[22:25], v[4:5], off offset:2048 nt
	s_nop 1
	v_add_co_u32_e32 v4, vcc, 0x4a000, v2
	s_nop 1
	v_addc_co_u32_e32 v5, vcc, 0, v3, vcc
	global_load_dwordx4 v[18:21], v[4:5], off offset:1024 nt
	s_nop 1
	v_add_co_u32_e32 v4, vcc, 0x4d000, v2
	s_nop 1
	v_addc_co_u32_e32 v5, vcc, 0, v3, vcc
	global_load_dwordx4 v[14:17], v[4:5], off nt
	s_nop 1
	v_add_co_u32_e32 v4, vcc, 0x4f000, v2
	s_nop 1
	v_addc_co_u32_e32 v5, vcc, 0, v3, vcc
	global_load_dwordx4 v[10:13], v[4:5], off offset:3072 nt
	s_nop 1
	v_add_co_u32_e32 v4, vcc, 0x52000, v2
	s_nop 1
	v_addc_co_u32_e32 v5, vcc, 0, v3, vcc
	v_add_co_u32_e32 v2, vcc, 0x55000, v2
	global_load_dwordx4 v[6:9], v[4:5], off offset:2048 nt
	s_nop 1
	v_addc_co_u32_e32 v3, vcc, 0, v3, vcc
	global_load_dwordx4 v[2:5], v[2:3], off offset:1024 nt
	s_nop 1
	s_nop 0
	s_nop 0
	s_nop 0
	s_waitcnt vmcnt(32)
	ds_bpermute_b32 v170, v138, v169
	s_waitcnt lgkmcnt(0)
	v_mul_f32_e32 v170, s13, v170
	s_nop 1
	v_mov_b32_e32 v172, v195
	s_nop 0
	s_nop 1
	v_mov_b32_e32 v173, v195
	s_nop 0
	s_waitcnt vmcnt(31)
	v_pk_mul_f32 v[128:129], v[128:129], v[170:171] op_sel_hi:[1,0]
	s_nop 1
	v_pk_mul_f32 v[126:127], v[126:127], v[170:171] op_sel_hi:[1,0]
	s_nop 0
	s_nop 1
	ds_bpermute_b32 v170, v139, v169
	s_nop 0
	s_waitcnt lgkmcnt(0)
	v_mul_f32_e32 v170, s13, v170
	s_waitcnt vmcnt(30)
	v_pk_mul_f32 v[124:125], v[124:125], v[170:171] op_sel_hi:[1,0]
	s_nop 1
	v_pk_mul_f32 v[122:123], v[122:123], v[170:171] op_sel_hi:[1,0]
	s_nop 0
	s_nop 1
	ds_bpermute_b32 v170, v140, v169
	s_nop 0
	s_waitcnt lgkmcnt(0)
	v_mul_f32_e32 v170, s13, v170
	s_waitcnt vmcnt(29)
	v_pk_mul_f32 v[120:121], v[120:121], v[170:171] op_sel_hi:[1,0]
	v_pk_mul_f32 v[118:119], v[118:119], v[170:171] op_sel_hi:[1,0]
	ds_bpermute_b32 v170, v141, v169
	s_nop 1
	s_lshl_b32 s8, s16, 2
	s_nop 0
	s_waitcnt lgkmcnt(0)
	v_mul_f32_e32 v170, s13, v170
	s_waitcnt vmcnt(28)
	v_pk_mul_f32 v[116:117], v[116:117], v[170:171] op_sel_hi:[1,0]
	v_pk_mul_f32 v[114:115], v[114:115], v[170:171] op_sel_hi:[1,0]
	ds_bpermute_b32 v170, v142, v169
	s_nop 1
	s_mov_b32 s16, 1
	s_nop 0
	s_waitcnt lgkmcnt(0)
	v_mul_f32_e32 v170, s13, v170
	s_waitcnt vmcnt(27)
	v_pk_mul_f32 v[112:113], v[112:113], v[170:171] op_sel_hi:[1,0]
	v_pk_mul_f32 v[110:111], v[110:111], v[170:171] op_sel_hi:[1,0]
	ds_bpermute_b32 v170, v143, v169
	s_waitcnt lgkmcnt(0)
	v_mul_f32_e32 v170, s13, v170
	s_waitcnt vmcnt(26)
	v_pk_mul_f32 v[108:109], v[108:109], v[170:171] op_sel_hi:[1,0]
	v_pk_mul_f32 v[106:107], v[106:107], v[170:171] op_sel_hi:[1,0]
	ds_bpermute_b32 v170, v144, v169
	s_waitcnt lgkmcnt(0)
	v_mul_f32_e32 v170, s13, v170
	s_waitcnt vmcnt(25)
	v_pk_mul_f32 v[104:105], v[104:105], v[170:171] op_sel_hi:[1,0]
	v_pk_mul_f32 v[102:103], v[102:103], v[170:171] op_sel_hi:[1,0]
	ds_bpermute_b32 v170, v145, v169
	s_waitcnt lgkmcnt(0)
	v_mul_f32_e32 v170, s13, v170
	s_waitcnt vmcnt(24)
	v_pk_mul_f32 v[100:101], v[100:101], v[170:171] op_sel_hi:[1,0]
	v_pk_mul_f32 v[98:99], v[98:99], v[170:171] op_sel_hi:[1,0]
	ds_bpermute_b32 v170, v146, v169
	s_waitcnt lgkmcnt(0)
	v_mul_f32_e32 v170, s13, v170
	s_waitcnt vmcnt(23)
	v_pk_mul_f32 v[96:97], v[96:97], v[170:171] op_sel_hi:[1,0]
	v_pk_mul_f32 v[94:95], v[94:95], v[170:171] op_sel_hi:[1,0]
	ds_bpermute_b32 v170, v147, v169
	s_waitcnt lgkmcnt(0)
	v_mul_f32_e32 v170, s13, v170
	s_waitcnt vmcnt(22)
	v_pk_mul_f32 v[92:93], v[92:93], v[170:171] op_sel_hi:[1,0]
	v_pk_mul_f32 v[90:91], v[90:91], v[170:171] op_sel_hi:[1,0]
	ds_bpermute_b32 v170, v148, v169
	s_nop 1
	v_cvt_pk_fp8_f32 v172, v94, v90
	s_nop 0
	s_waitcnt lgkmcnt(0)
	v_mul_f32_e32 v170, s13, v170
	s_waitcnt vmcnt(21)
	v_pk_mul_f32 v[88:89], v[88:89], v[170:171] op_sel_hi:[1,0]
	v_pk_mul_f32 v[86:87], v[86:87], v[170:171] op_sel_hi:[1,0]
	ds_bpermute_b32 v170, v149, v169
	s_waitcnt lgkmcnt(0)
	v_mul_f32_e32 v170, s13, v170
	s_waitcnt vmcnt(20)
	v_pk_mul_f32 v[84:85], v[84:85], v[170:171] op_sel_hi:[1,0]
	v_pk_mul_f32 v[82:83], v[82:83], v[170:171] op_sel_hi:[1,0]
	ds_bpermute_b32 v170, v150, v169
	s_nop 1
	v_cvt_pk_fp8_f32 v172, v86, v82 op_sel:[0,0,1]
	s_nop 0
	s_waitcnt lgkmcnt(0)
	v_mul_f32_e32 v170, s13, v170
	s_waitcnt vmcnt(19)
	v_pk_mul_f32 v[80:81], v[80:81], v[170:171] op_sel_hi:[1,0]
	v_pk_mul_f32 v[78:79], v[78:79], v[170:171] op_sel_hi:[1,0]
	ds_bpermute_b32 v170, v151, v169
	s_nop 1
	v_mov_b32_e32 v82, v195
	s_nop 0
	s_waitcnt lgkmcnt(0)
	v_mul_f32_e32 v170, s13, v170
	s_waitcnt vmcnt(18)
	v_pk_mul_f32 v[76:77], v[76:77], v[170:171] op_sel_hi:[1,0]
	v_pk_mul_f32 v[74:75], v[74:75], v[170:171] op_sel_hi:[1,0]
	ds_bpermute_b32 v170, v152, v169
	s_nop 1
	v_cvt_pk_fp8_f32 v173, v78, v74
	s_nop 0
	s_waitcnt lgkmcnt(0)
	v_mul_f32_e32 v170, s13, v170
	s_waitcnt vmcnt(17)
	v_pk_mul_f32 v[72:73], v[72:73], v[170:171] op_sel_hi:[1,0]
	v_pk_mul_f32 v[70:71], v[70:71], v[170:171] op_sel_hi:[1,0]
	ds_bpermute_b32 v170, v153, v169
	s_nop 1
	v_cvt_pk_fp8_f32 v82, v129, v125
	s_nop 0
	s_waitcnt lgkmcnt(0)
	v_mul_f32_e32 v170, s13, v170
	s_waitcnt vmcnt(16)
	v_pk_mul_f32 v[68:69], v[68:69], v[170:171] op_sel_hi:[1,0]
	v_pk_mul_f32 v[66:67], v[66:67], v[170:171] op_sel_hi:[1,0]
	ds_bpermute_b32 v170, v154, v169
	s_nop 1
	v_cvt_pk_fp8_f32 v173, v70, v66 op_sel:[0,0,1]
	s_nop 0
	s_waitcnt lgkmcnt(0)
	v_mul_f32_e32 v170, s13, v170
	s_waitcnt vmcnt(15)
	v_pk_mul_f32 v[64:65], v[64:65], v[170:171] op_sel_hi:[1,0]
	v_pk_mul_f32 v[62:63], v[62:63], v[170:171] op_sel_hi:[1,0]
	ds_bpermute_b32 v170, v155, v169
	s_nop 1
	v_bitop3_b32 v66, s8, v133, v134 bitop3:0x36
	s_nop 0
	s_nop 0
	s_waitcnt lgkmcnt(0)
	v_mul_f32_e32 v170, s13, v170
	s_waitcnt vmcnt(14)
	v_pk_mul_f32 v[60:61], v[60:61], v[170:171] op_sel_hi:[1,0]
	v_pk_mul_f32 v[58:59], v[58:59], v[170:171] op_sel_hi:[1,0]
	ds_bpermute_b32 v170, v156, v169
	v_lshl_add_u32 v66, v66, 4, v137
	v_cvt_pk_fp8_f32 v82, v121, v117 op_sel:[0,0,1]
	s_andn2_b64 vcc, exec, s[6:7]
	s_waitcnt lgkmcnt(0)
	v_mul_f32_e32 v170, s13, v170
	s_waitcnt vmcnt(13)
	v_pk_mul_f32 v[56:57], v[56:57], v[170:171] op_sel_hi:[1,0]
	v_pk_mul_f32 v[54:55], v[54:55], v[170:171] op_sel_hi:[1,0]
	ds_bpermute_b32 v170, v157, v169
	s_waitcnt lgkmcnt(0)
	v_mul_f32_e32 v170, s13, v170
	s_waitcnt vmcnt(12)
	v_pk_mul_f32 v[52:53], v[52:53], v[170:171] op_sel_hi:[1,0]
	v_pk_mul_f32 v[50:51], v[50:51], v[170:171] op_sel_hi:[1,0]
	ds_bpermute_b32 v170, v158, v169
	s_waitcnt lgkmcnt(0)
	v_mul_f32_e32 v170, s13, v170
	s_waitcnt vmcnt(11)
	v_pk_mul_f32 v[48:49], v[48:49], v[170:171] op_sel_hi:[1,0]
	v_pk_mul_f32 v[46:47], v[46:47], v[170:171] op_sel_hi:[1,0]
	ds_bpermute_b32 v170, v159, v169
	s_waitcnt lgkmcnt(0)
	v_mul_f32_e32 v170, s13, v170
	s_waitcnt vmcnt(10)
	v_pk_mul_f32 v[44:45], v[44:45], v[170:171] op_sel_hi:[1,0]
	v_pk_mul_f32 v[42:43], v[42:43], v[170:171] op_sel_hi:[1,0]
	ds_bpermute_b32 v170, v160, v169
	s_waitcnt lgkmcnt(0)
	v_mul_f32_e32 v170, s13, v170
	s_waitcnt vmcnt(9)
	v_pk_mul_f32 v[40:41], v[40:41], v[170:171] op_sel_hi:[1,0]
	v_pk_mul_f32 v[38:39], v[38:39], v[170:171] op_sel_hi:[1,0]
	ds_bpermute_b32 v170, v161, v169
	s_waitcnt lgkmcnt(0)
	v_mul_f32_e32 v170, s13, v170
	s_waitcnt vmcnt(8)
	v_pk_mul_f32 v[36:37], v[36:37], v[170:171] op_sel_hi:[1,0]
	v_pk_mul_f32 v[34:35], v[34:35], v[170:171] op_sel_hi:[1,0]
	ds_bpermute_b32 v170, v162, v169
	s_waitcnt lgkmcnt(0)
	v_mul_f32_e32 v170, s13, v170
	s_waitcnt vmcnt(7)
	v_pk_mul_f32 v[32:33], v[32:33], v[170:171] op_sel_hi:[1,0]
	v_pk_mul_f32 v[30:31], v[30:31], v[170:171] op_sel_hi:[1,0]
	ds_bpermute_b32 v170, v163, v169
	s_waitcnt lgkmcnt(0)
	v_mul_f32_e32 v170, s13, v170
	s_waitcnt vmcnt(6)
	v_pk_mul_f32 v[28:29], v[28:29], v[170:171] op_sel_hi:[1,0]
	v_pk_mul_f32 v[26:27], v[26:27], v[170:171] op_sel_hi:[1,0]
	ds_bpermute_b32 v170, v164, v169
	s_waitcnt lgkmcnt(0)
	v_mul_f32_e32 v170, s13, v170
	s_waitcnt vmcnt(5)
	v_pk_mul_f32 v[24:25], v[24:25], v[170:171] op_sel_hi:[1,0]
	v_pk_mul_f32 v[22:23], v[22:23], v[170:171] op_sel_hi:[1,0]
	ds_bpermute_b32 v170, v165, v169
	s_waitcnt lgkmcnt(0)
	v_mul_f32_e32 v170, s13, v170
	s_waitcnt vmcnt(4)
	v_pk_mul_f32 v[20:21], v[20:21], v[170:171] op_sel_hi:[1,0]
	v_pk_mul_f32 v[18:19], v[18:19], v[170:171] op_sel_hi:[1,0]
	ds_bpermute_b32 v170, v166, v169
	s_waitcnt lgkmcnt(0)
	v_mul_f32_e32 v170, s13, v170
	s_waitcnt vmcnt(3)
	v_pk_mul_f32 v[16:17], v[16:17], v[170:171] op_sel_hi:[1,0]
	v_pk_mul_f32 v[14:15], v[14:15], v[170:171] op_sel_hi:[1,0]
	ds_bpermute_b32 v170, v167, v169
	s_waitcnt lgkmcnt(0)
	v_mul_f32_e32 v170, s13, v170
	s_waitcnt vmcnt(2)
	v_pk_mul_f32 v[12:13], v[12:13], v[170:171] op_sel_hi:[1,0]
	v_pk_mul_f32 v[10:11], v[10:11], v[170:171] op_sel_hi:[1,0]
	ds_bpermute_b32 v170, v168, v169
	ds_bpermute_b32 v169, v136, v169
	s_waitcnt lgkmcnt(1)
	v_mul_f32_e32 v170, s13, v170
	s_waitcnt vmcnt(1)
	v_pk_mul_f32 v[8:9], v[8:9], v[170:171] op_sel_hi:[1,0]
	v_pk_mul_f32 v[6:7], v[6:7], v[170:171] op_sel_hi:[1,0]
	s_waitcnt lgkmcnt(0)
	v_mul_f32_e32 v170, s13, v169
	s_waitcnt vmcnt(0)
	v_pk_mul_f32 v[4:5], v[4:5], v[170:171] op_sel_hi:[1,0]
	v_pk_mul_f32 v[2:3], v[2:3], v[170:171] op_sel_hi:[1,0]
	v_mov_b32_e32 v170, v195
	v_mov_b32_e32 v171, v195
	v_cvt_pk_fp8_f32 v170, v126, v122
	v_cvt_pk_fp8_f32 v171, v110, v106
	v_or_b32_e32 v169, s8, v134
	s_mov_b64 s[8:9], 0
	v_cvt_pk_fp8_f32 v170, v118, v114 op_sel:[0,0,1]
	v_cvt_pk_fp8_f32 v171, v102, v98 op_sel:[0,0,1]
	ds_write_b128 v66, v[170:173]
	v_mov_b32_e32 v170, v195
	v_mov_b32_e32 v171, v195
	v_mov_b32_e32 v172, v195
	v_mov_b32_e32 v173, v195
	v_cvt_pk_fp8_f32 v170, v62, v58
	v_cvt_pk_fp8_f32 v171, v46, v42
	v_cvt_pk_fp8_f32 v172, v30, v26
	v_cvt_pk_fp8_f32 v173, v14, v10
	v_cvt_pk_fp8_f32 v170, v54, v50 op_sel:[0,0,1]
	v_cvt_pk_fp8_f32 v171, v38, v34 op_sel:[0,0,1]
	v_cvt_pk_fp8_f32 v172, v22, v18 op_sel:[0,0,1]
	v_cvt_pk_fp8_f32 v173, v6, v2 op_sel:[0,0,1]
	v_bitop3_b32 v2, v169, v133, 1 bitop3:0x36
	v_lshl_add_u32 v2, v2, 4, v137
	v_mov_b32_e32 v18, v195
	ds_write_b128 v2, v[170:173]
	v_mov_b32_e32 v170, v195
	v_mov_b32_e32 v171, v195
	v_mov_b32_e32 v172, v195
	v_mov_b32_e32 v173, v195
	v_cvt_pk_fp8_f32 v170, v127, v123
	v_cvt_pk_fp8_f32 v171, v111, v107
	v_cvt_pk_fp8_f32 v172, v95, v91
	v_cvt_pk_fp8_f32 v173, v79, v75
	v_cvt_pk_fp8_f32 v170, v119, v115 op_sel:[0,0,1]
	v_cvt_pk_fp8_f32 v171, v103, v99 op_sel:[0,0,1]
	v_cvt_pk_fp8_f32 v172, v87, v83 op_sel:[0,0,1]
	v_cvt_pk_fp8_f32 v173, v71, v67 op_sel:[0,0,1]
	v_mov_b32_e32 v83, v195
	v_cvt_pk_fp8_f32 v83, v113, v109
	v_cvt_pk_fp8_f32 v18, v65, v61
	ds_write_b128 v66, v[170:173] offset:128
	v_mov_b32_e32 v170, v195
	v_mov_b32_e32 v171, v195
	v_mov_b32_e32 v172, v195
	v_mov_b32_e32 v173, v195
	v_cvt_pk_fp8_f32 v170, v63, v59
	v_cvt_pk_fp8_f32 v171, v47, v43
	v_cvt_pk_fp8_f32 v172, v31, v27
	v_cvt_pk_fp8_f32 v173, v15, v11
	v_cvt_pk_fp8_f32 v170, v55, v51 op_sel:[0,0,1]
	v_cvt_pk_fp8_f32 v171, v39, v35 op_sel:[0,0,1]
	v_cvt_pk_fp8_f32 v172, v23, v19 op_sel:[0,0,1]
	v_cvt_pk_fp8_f32 v173, v7, v3 op_sel:[0,0,1]
	v_mov_b32_e32 v19, v195
	v_cvt_pk_fp8_f32 v19, v49, v45
	v_cvt_pk_fp8_f32 v83, v105, v101 op_sel:[0,0,1]
	ds_write_b128 v2, v[170:173] offset:128
	v_mov_b32_e32 v170, v195
	v_mov_b32_e32 v171, v195
	v_mov_b32_e32 v172, v195
	v_mov_b32_e32 v173, v195
	v_cvt_pk_fp8_f32 v170, v128, v124
	v_cvt_pk_fp8_f32 v171, v112, v108
	v_cvt_pk_fp8_f32 v172, v96, v92
	v_cvt_pk_fp8_f32 v173, v80, v76
	v_cvt_pk_fp8_f32 v170, v120, v116 op_sel:[0,0,1]
	v_cvt_pk_fp8_f32 v171, v104, v100 op_sel:[0,0,1]
	v_cvt_pk_fp8_f32 v172, v88, v84 op_sel:[0,0,1]
	v_cvt_pk_fp8_f32 v173, v72, v68 op_sel:[0,0,1]
	v_mov_b32_e32 v84, v195
	v_cvt_pk_fp8_f32 v84, v97, v93
	v_cvt_pk_fp8_f32 v18, v57, v53 op_sel:[0,0,1]
	ds_write_b128 v66, v[170:173] offset:256
	v_mov_b32_e32 v172, v195
	v_cvt_pk_fp8_f32 v172, v32, v28
	v_mov_b32_e32 v170, v195
	v_mov_b32_e32 v171, v195
	v_mov_b32_e32 v173, v195
	v_cvt_pk_fp8_f32 v172, v24, v20 op_sel:[0,0,1]
	v_mov_b32_e32 v20, v195
	v_cvt_pk_fp8_f32 v20, v33, v29
	v_cvt_pk_fp8_f32 v84, v89, v85 op_sel:[0,0,1]
	v_mov_b32_e32 v85, v195
	v_cvt_pk_fp8_f32 v170, v64, v60
	v_cvt_pk_fp8_f32 v20, v25, v21 op_sel:[0,0,1]
	v_mov_b32_e32 v21, v195
	v_cvt_pk_fp8_f32 v171, v48, v44
	v_cvt_pk_fp8_f32 v173, v16, v12
	v_cvt_pk_fp8_f32 v85, v81, v77
	v_cvt_pk_fp8_f32 v21, v17, v13
	v_cvt_pk_fp8_f32 v170, v56, v52 op_sel:[0,0,1]
	v_cvt_pk_fp8_f32 v171, v40, v36 op_sel:[0,0,1]
	v_cvt_pk_fp8_f32 v173, v8, v4 op_sel:[0,0,1]
	v_cvt_pk_fp8_f32 v85, v73, v69 op_sel:[0,0,1]
	v_cvt_pk_fp8_f32 v19, v41, v37 op_sel:[0,0,1]
	v_cvt_pk_fp8_f32 v21, v9, v5 op_sel:[0,0,1]
	ds_write_b128 v2, v[170:173] offset:256
	ds_write_b128 v66, v[82:85] offset:384
	ds_write_b128 v2, v[18:21] offset:384
	s_cbranch_vccz .LBB0_892
